# stack9: stack8 + expert phase requests the first k-step's weight fragments before the gather
# speedup vs baseline: 1.0016x; 1.0016x over previous
; #define LD32(p_) CAT8(*(const i32x4v*)(p_), *(const i32x4v*)((p_) + 16))
; DEVINL void phase5(const Params& P, unsigned char* smem) {
;     ...
;     for (int it = vb; it < total; it += G) {
;         int cls = 0;
; #pragma unroll
;         for (int st = 64; st >= 1; st >>= 1) if (cls + st <= 111 && s_cp[cls + st] <= it) cls += st;
;         const int mt = it - s_cp[cls], cc = s_cv[cls], ntl = s_cp[cls + 1] - s_cp[cls], rpt = (cc + ntl - 1) / ntl;
;         const int rbeg = mt * rpt, rend = (rbeg + rpt < cc) ? rbeg + rpt : cc;
;         const int grp = cls / 28, pidx = cls - grp * 28;
;         int ilo = 0; for (; ilo < 7; ++ilo) { const int b_ = ilo * (15 - ilo) / 2; if (pidx < b_ + 7 - ilo) break; }
;         const int e_lo = grp * 8 + ilo, e_hi = grp * 8 + ilo + 1 + (pidx - ilo * (15 - ilo) / 2);
;         t = t0_; asm volatile("" : "+v"(t));
;         int lane = t & 63;
;         const int lr = lane & 15, g = lane >> 4;
;         unsigned voff = (unsigned)(lane * 32);
;         asm volatile("" : "+v"(voff));
;         __syncthreads();
;         {
; #pragma unroll
;             for (int rp = 0; rp < 2; ++rp) {
;                 const int row = (t >> 3) + 64 * rp, r = rbeg + row;
;                 if (row < 80) {
;                     const bool ok = r < rend;
;                     const int tok = ok ? ctok[cls * NT + r] : 0; const f32x2 w2 = ok ? cw[cls * NT + r] : (f32x2){0.f, 0.f};
;                     if ((t & 7) == 0) { s_tok[row] = ok ? tok : -1; s_wl[row] = w2.x; s_wh[row] = w2.y; }
;                     const unsigned char* src = H2 + (size_t)tok * DM;
; #pragma unroll
;                     for (int i = 0; i < 8; ++i) { const int c = (t & 7) + 8 * i; *(u32x4*)(smem + row * 1024 + ((c ^ (row & 15)) << 4)) = *(const u32x4*)(src + c * 16); }
;                 }
;             }
;         }
;         __syncthreads();
;         i32x8 b0[4];
; #pragma unroll
;         for (int j_ = 0; j_ < 4; ++j_) b0[j_] = LD32(P.ws + WS_WGUF + (size_t)e_lo * (8 * 32 * 2048) + (size_t)(4 * wv) * 2048 + j_ * 2048 + voff);
.LBB0_704:
	s_sub_i32 s29, s29, s28
	s_abs_i32 s30, s29
	v_cvt_f32_u32_e32 v2, s30
	s_add_i32 s31, s1, s29
	s_add_i32 s49, s31, -1
	s_sub_i32 s31, 1, s31
	v_rcp_iflag_f32_e32 v2, v2
	s_sub_i32 s51, 0, s30
	s_xor_b32 s29, s49, s29
	s_max_i32 s31, s49, s31
	v_mul_f32_e32 v2, 0x4f7ffffe, v2
	v_cvt_u32_f32_e32 v2, v2
	s_sub_i32 s28, s80, s28
	s_ashr_i32 s29, s29, 31
	v_mov_b32_e32 v34, v0
	v_readfirstlane_b32 s49, v2
	s_mul_i32 s51, s51, s49
	s_mul_hi_u32 s51, s49, s51
	s_add_i32 s49, s49, s51
	s_mul_hi_u32 s49, s31, s49
	s_mul_i32 s51, s49, s30
	s_sub_i32 s31, s31, s51
	s_add_i32 s52, s49, 1
	s_sub_i32 s51, s31, s30
	s_cmp_ge_u32 s31, s30
	s_cselect_b32 s49, s52, s49
	s_cselect_b32 s31, s51, s31
	s_add_i32 s51, s49, 1
	s_cmp_ge_u32 s31, s30
	s_cselect_b32 s30, s51, s49
	s_xor_b32 s30, s30, s29
	s_sub_i32 s29, s30, s29
	s_mul_i32 s49, s29, s28
	s_add_i32 s28, s49, s29
	s_min_i32 s51, s28, s1
	v_and_b32_e32 v223, 63, v34
	v_ashrrev_i32_e32 v12, 3, v34
	v_and_b32_e32 v10, 7, v34
	v_lshlrev_b32_e32 v194, 5, v223
	s_lshl_b32 s52, s0, 14
	v_cmp_eq_u32_e32 vcc, 0, v10
	v_and_b32_e32 v11, 15, v12
	v_cmp_gt_i32_e64 s[0:1], s43, v12
	s_barrier
	v_mov_b32_e32 v146, v10
	v_mov_b32_e32 v147, v11
	v_mov_b32_e32 v148, v12
	s_lshl_b32 s60, s35, 3
	s_or_b32 s64, s50, s60
	s_xor_b32 s60, s50, 15
	s_mul_i32 s60, s60, s50
	s_lshr_b32 s60, s60, 1
	s_add_i32 s65, s34, s64
	s_sub_i32 s65, s65, s60
	s_add_i32 s65, s65, 1
	s_lshl_b32 s60, s64, 19
	s_add_u32 s60, s37, s60
	s_addc_u32 s61, s38, 0
	s_add_u32 s62, s60, 0x1000
	s_addc_u32 s63, s61, 0
	global_load_dwordx4 v[2:5], v194, s[60:61]
	global_load_dwordx4 v[6:9], v194, s[60:61] offset:16
	global_load_dwordx4 v[10:13], v194, s[60:61] offset:2048
	global_load_dwordx4 v[14:17], v194, s[60:61] offset:2064
	global_load_dwordx4 v[18:21], v194, s[62:63]
	global_load_dwordx4 v[22:25], v194, s[62:63] offset:16
	global_load_dwordx4 v[26:29], v194, s[62:63] offset:2048
	global_load_dwordx4 v[30:33], v194, s[62:63] offset:2064
	v_add_u32_e32 v50, s49, v148
	s_add_i32 s94, s51, -1
	v_add_u32_e32 v51, 64, v50
	v_cmp_gt_i32_e64 s[82:83], s51, v50
	v_min_i32_e32 v52, s94, v50
	v_min_i32_e32 v53, s94, v51
	v_cmp_gt_i32_e64 s[86:87], s51, v51
	v_add_u32_e32 v52, s52, v52
	v_add_u32_e32 v53, s52, v53
	v_lshlrev_b32_e32 v60, 2, v52
	v_lshlrev_b32_e32 v61, 2, v53
	v_lshlrev_b32_e32 v62, 3, v52
	v_lshlrev_b32_e32 v63, 3, v53
	global_load_dword v54, v60, s[6:7]
	global_load_dword v55, v61, s[6:7]
	global_load_dwordx2 v[56:57], v62, s[8:9]
	global_load_dwordx2 v[58:59], v63, s[8:9]
	v_readfirstlane_b32 s95, v148
	v_lshl_add_u32 v130, v148, 10, 0
	v_xor_b32_e32 v131, v147, v146
	v_bitop3_b32 v132, v146, v147, 8 bitop3:0x36
	v_bitop3_b32 v133, v146, v147, 16 bitop3:0x36
	v_bitop3_b32 v134, v146, v147, 24 bitop3:0x36
	v_bitop3_b32 v135, v146, v147, 32 bitop3:0x36
	v_bitop3_b32 v136, v146, v147, 40 bitop3:0x36
	v_bitop3_b32 v137, v146, v147, 48 bitop3:0x36
	v_bitop3_b32 v138, v146, v147, 56 bitop3:0x36
	v_lshl_add_u32 v131, v131, 4, v130
	v_lshl_add_u32 v132, v132, 4, v130
	v_lshl_add_u32 v133, v133, 4, v130
	v_lshl_add_u32 v134, v134, 4, v130
	v_lshl_add_u32 v135, v135, 4, v130
	v_lshl_add_u32 v136, v136, 4, v130
	v_lshl_add_u32 v137, v137, 4, v130
	v_lshl_add_u32 v138, v138, 4, v130
	v_lshl_add_u32 v140, v148, 2, 0
	v_cmp_eq_u32_e64 s[90:91], 0, v146
	v_cmp_gt_i32_e64 s[92:93], 16, v148
	s_waitcnt vmcnt(2)
	v_lshlrev_b32_e32 v64, 10, v54
	v_lshlrev_b32_e32 v65, 10, v55
	v_lshl_or_b32 v64, v146, 4, v64
	v_lshl_or_b32 v65, v146, 4, v65
	global_load_dwordx4 v[66:69], v64, s[4:5]
	global_load_dwordx4 v[70:73], v64, s[4:5] offset:128
	global_load_dwordx4 v[74:77], v64, s[4:5] offset:256
	global_load_dwordx4 v[78:81], v64, s[4:5] offset:384
	global_load_dwordx4 v[82:85], v64, s[4:5] offset:512
	global_load_dwordx4 v[86:89], v64, s[4:5] offset:640
	global_load_dwordx4 v[90:93], v64, s[4:5] offset:768
	global_load_dwordx4 v[94:97], v64, s[4:5] offset:896
	s_cmp_lt_u32 s95, 16
	s_cbranch_scc0 .Lp5_g_norows1
	global_load_dwordx4 v[98:101], v65, s[4:5]
	global_load_dwordx4 v[102:105], v65, s[4:5] offset:128
	global_load_dwordx4 v[106:109], v65, s[4:5] offset:256
	global_load_dwordx4 v[110:113], v65, s[4:5] offset:384
	global_load_dwordx4 v[114:117], v65, s[4:5] offset:512
	global_load_dwordx4 v[118:121], v65, s[4:5] offset:640
	global_load_dwordx4 v[122:125], v65, s[4:5] offset:768
	global_load_dwordx4 v[126:129], v65, s[4:5] offset:896

; #define LD32(p_) CAT8(*(const i32x4v*)(p_), *(const i32x4v*)((p_) + 16))
; DEVINL void phase5(const Params& P, unsigned char* smem) {
;     ...
;         for (int j_ = 0; j_ < 4; ++j_) b0[j_] = LD32(P.ws + WS_WGUF + (size_t)e_lo * (8 * 32 * 2048) + (size_t)(4 * wv) * 2048 + j_ * 2048 + voff);
; #pragma unroll 1
;         for (int sx = 0; sx < 2; ++sx) {
;             const int e = sx ? e_hi : e_lo;
;             f32x4 acc[4][5];
; #pragma unroll
;             for (int i = 0; i < 4; ++i)
; #pragma unroll
;                 for (int mi = 0; mi < 5; ++mi) acc[i][mi] = (f32x4){0.f, 0.f, 0.f, 0.f};
;             const unsigned char* wb1 = P.ws + WS_WGUF + (size_t)e * (8 * 32 * 2048) + (size_t)(4 * wv) * 2048;
;             const int aoff = lr * 1024;
;     ...
;             const unsigned char* nxt_ = sx ? P.ws + WS_WDF + (size_t)e_lo * (2 * 64 * 2048) + (size_t)(8 * wv) * 2048 : P.ws + WS_WGUF + (size_t)e_hi * (8 * 32 * 2048) + (size_t)(4 * wv) * 2048;
.Lp5_g_skipw1:
	s_mov_b64 exec, s[82:83]
	s_mov_b32 s49, s64
	s_mov_b32 s0, s65
	s_lshl_b32 s60, s64, 18
	s_add_u32 s1, s39, s60
	s_addc_u32 s50, s40, 0
	s_lshl_b32 s60, s65, 19
	s_add_u32 s51, s37, s60
	s_addc_u32 s52, s38, 0
	s_mov_b32 s53, 0
	s_mov_b64 s[30:31], -1
	v_and_b32_e32 v114, 15, v223
	v_lshrrev_b32_e32 v116, 3, v223
	v_lshl_add_u32 v115, v114, 10, 0
	v_and_b32_e32 v116, 6, v116
	v_add_u32_e32 v117, 0x10000, v115
	s_waitcnt lgkmcnt(0)
	s_barrier
